# baseline (speedup 1.0000x reference)
.LBB3_2:
	v_add_u32_e32 v206, s27, v214
	ds_read_b64_tr_b16 v[194:195], v206 offset:24576
	ds_read_b64_tr_b16 v[196:197], v206 offset:25088
	s_waitcnt lgkmcnt(9)
	v_mfma_f32_32x32x16_bf16 v[114:129], v[190:193], v[158:161], v[50:65]
	v_add_f32_e32 v98, v82, v83
	v_add_f32_e32 v98, v84, v98
	v_add_f32_e32 v98, v85, v98
	v_add_f32_e32 v98, v86, v98
	v_add_f32_e32 v130, v87, v98
	v_cvt_pk_bf16_f32 v142, v82, v83
	v_cvt_pk_bf16_f32 v143, v84, v85
	ds_read_b64_tr_b16 v[190:191], v206 offset:28672
	ds_read_b64_tr_b16 v[192:193], v206 offset:29184
	v_add_f32_e32 v82, v88, v130
	v_add_f32_e32 v82, v89, v82
	s_waitcnt lgkmcnt(10)
	v_mfma_f32_32x32x16_bf16 v[98:113], v[186:189], v[158:161], v[50:65]
	v_add_f32_e32 v82, v90, v82
	v_add_f32_e32 v82, v91, v82
	v_cvt_pk_bf16_f32 v144, v86, v87
	v_cvt_pk_bf16_f32 v145, v88, v89
	ds_read_b64_tr_b16 v[186:187], v206 offset:25600
	ds_read_b64_tr_b16 v[188:189], v206 offset:26112
	s_waitcnt lgkmcnt(11)
	v_mfma_f32_32x32x16_bf16 v[114:129], v[182:185], v[154:157], v[114:129]
	v_add_f32_e32 v82, v92, v82
	v_add_f32_e32 v82, v93, v82
	v_add_f32_e32 v82, v94, v82
	v_add_f32_e32 v82, v95, v82
	v_cvt_pk_bf16_f32 v138, v90, v91
	v_cvt_pk_bf16_f32 v139, v92, v93
	ds_read_b64_tr_b16 v[86:87], v206 offset:29696
	ds_read_b64_tr_b16 v[88:89], v206 offset:30208
	s_waitcnt lgkmcnt(12)
	v_mfma_f32_32x32x16_bf16 v[98:113], v[178:181], v[154:157], v[98:113]
	v_add_f32_e32 v82, v96, v82
	v_add_f32_e32 v82, v97, v82
	v_add_f32_e32 v82, v66, v82
	v_add_f32_e32 v90, v67, v82
	v_cvt_pk_bf16_f32 v140, v94, v95
	v_cvt_pk_bf16_f32 v141, v96, v97
	ds_read_b64_tr_b16 v[82:83], v206 offset:26624
	ds_read_b64_tr_b16 v[84:85], v206 offset:27136
	s_waitcnt lgkmcnt(13)
	v_mfma_f32_32x32x16_bf16 v[114:129], v[174:177], v[150:153], v[114:129]
	v_add_f32_e32 v90, v68, v90
	v_add_f32_e32 v90, v69, v90
	v_add_f32_e32 v90, v70, v90
	v_add_f32_e32 v90, v71, v90
	v_cvt_pk_bf16_f32 v134, v66, v67
	v_cvt_pk_bf16_f32 v135, v68, v69
	ds_read_b64_tr_b16 v[66:67], v206 offset:30720
	ds_read_b64_tr_b16 v[68:69], v206 offset:31232
	s_waitcnt lgkmcnt(14)
	v_mfma_f32_32x32x16_bf16 v[98:113], v[170:173], v[150:153], v[98:113]
	v_add_f32_e32 v90, v72, v90
	v_add_f32_e32 v90, v73, v90
	v_add_f32_e32 v90, v74, v90
	v_add_f32_e32 v90, v75, v90
	v_cvt_pk_bf16_f32 v136, v70, v71
	v_cvt_pk_bf16_f32 v137, v72, v73
	ds_read_b64_tr_b16 v[70:71], v206 offset:27648
	ds_read_b64_tr_b16 v[72:73], v206 offset:28160
	s_waitcnt lgkmcnt(14)
	v_mfma_f32_32x32x16_bf16 v[114:129], v[166:169], v[146:149], v[114:129]
	v_add_f32_e32 v90, v76, v90
	v_add_f32_e32 v90, v77, v90
	v_add_f32_e32 v90, v78, v90
	v_add_f32_e32 v90, v79, v90
	v_cvt_pk_bf16_f32 v130, v74, v75
	v_cvt_pk_bf16_f32 v131, v76, v77
	ds_read_b64_tr_b16 v[74:75], v206 offset:31744
	ds_read_b64_tr_b16 v[76:77], v206 offset:32256
	v_mfma_f32_32x32x16_bf16 v[98:113], v[162:165], v[146:149], v[98:113]
	v_add_f32_e32 v90, v80, v90
	v_add_f32_e32 v90, v81, v90
	v_cvt_pk_bf16_f32 v132, v78, v79
	v_cvt_pk_bf16_f32 v133, v80, v81
	s_nop 0
	v_lshl_add_u64 v[78:79], v[204:205], 0, s[24:25]
	s_add_i32 s26, s39, s35
	s_mov_b32 m0, s26
	s_nop 0
	global_load_lds_dwordx4 v[78:79], off
	v_max_f32_e32 v78, v115, v115
	v_max_f32_e32 v79, v114, v114
	v_max_f32_e32 v78, v79, v78
	s_nop 2
	v_max3_f32 v79, v116, v117, v99
	v_max3_f32 v78, v78, v98, v100
	v_max3_f32 v78, v78, v101, v118
	v_max3_f32 v79, v79, v120, v121
	v_max3_f32 v78, v78, v119, v102
	v_max3_f32 v79, v79, v104, v105
	v_max3_f32 v78, v78, v103, v122
	v_max3_f32 v79, v79, v124, v125
	v_max3_f32 v78, v78, v123, v106
	v_max3_f32 v79, v79, v108, v109
	v_max3_f32 v78, v78, v107, v126
	v_max3_f32 v79, v79, v128, v129
	v_max3_f32 v78, v78, v127, v110
	v_max3_f32 v79, v79, v112, v113
	v_max3_f32 v78, v78, v111, v79
	v_mov_b32_e32 v79, v78
	s_nop 1
	v_permlane32_swap_b32_e32 v78, v79
	v_max_f32_e32 v79, v79, v79
	v_max_f32_e32 v78, v78, v78
	v_max_f32_e32 v78, v78, v79
	v_lshl_add_u64 v[206:207], v[208:209], 0, s[18:19]
	s_add_i32 s26, s38, s34
	s_mov_b32 m0, s26
	s_nop 0
	global_load_lds_dwordx4 v[206:207], off
	v_cmp_lt_f32_e32 vcc, s15, v78
	s_cmp_lg_u64 vcc, 0
	v_add_f32_e32 v201, v201, v90
	s_cselect_b64 s[26:27], -1, 0
	s_cbranch_vccnz .LBB3_11

.LBB3_6:
	s_add_i32 s26, s38, 0x2000
	s_cmpk_lg_i32 s38, 0x4000
	s_cselect_b32 s40, s26, 0
	v_add_u32_e32 v217, s39, v214
	ds_read_b64_tr_b16 v[162:163], v217 offset:24576
	ds_read_b64_tr_b16 v[164:165], v217 offset:25088
	s_waitcnt lgkmcnt(9)
	v_mfma_f32_32x32x16_bf16 v[82:97], v[78:81], v[158:161], v[50:65]
	v_add_f32_e32 v66, v114, v115
	v_add_f32_e32 v66, v116, v66
	v_add_f32_e32 v66, v117, v66
	v_add_f32_e32 v66, v118, v66
	v_add_f32_e32 v66, v119, v66
	v_cvt_pk_bf16_f32 v142, v114, v115
	v_cvt_pk_bf16_f32 v143, v116, v117
	ds_read_b64_tr_b16 v[170:171], v217 offset:28672
	ds_read_b64_tr_b16 v[172:173], v217 offset:29184
	v_add_f32_e32 v66, v120, v66
	v_add_f32_e32 v66, v121, v66
	v_add_f32_e32 v66, v122, v66
	v_add_f32_e32 v114, v123, v66
	s_waitcnt lgkmcnt(10)
	v_mfma_f32_32x32x16_bf16 v[66:81], v[166:169], v[158:161], v[50:65]
	v_cvt_pk_bf16_f32 v144, v118, v119
	v_cvt_pk_bf16_f32 v145, v120, v121
	ds_read_b64_tr_b16 v[166:167], v217 offset:25600
	ds_read_b64_tr_b16 v[168:169], v217 offset:26112
	s_waitcnt lgkmcnt(11)
	v_mfma_f32_32x32x16_bf16 v[82:97], v[194:197], v[154:157], v[82:97]
	v_add_f32_e32 v114, v124, v114
	v_add_f32_e32 v114, v125, v114
	v_add_f32_e32 v114, v126, v114
	v_add_f32_e32 v114, v127, v114
	v_cvt_pk_bf16_f32 v138, v122, v123
	v_cvt_pk_bf16_f32 v139, v124, v125
	ds_read_b64_tr_b16 v[118:119], v217 offset:29696
	ds_read_b64_tr_b16 v[120:121], v217 offset:30208
	s_waitcnt lgkmcnt(12)
	v_mfma_f32_32x32x16_bf16 v[66:81], v[190:193], v[154:157], v[66:81]
	v_add_f32_e32 v114, v128, v114
	v_add_f32_e32 v114, v129, v114
	v_add_f32_e32 v114, v98, v114
	v_add_f32_e32 v122, v99, v114
	v_cvt_pk_bf16_f32 v140, v126, v127
	v_cvt_pk_bf16_f32 v141, v128, v129
	ds_read_b64_tr_b16 v[114:115], v217 offset:26624
	ds_read_b64_tr_b16 v[116:117], v217 offset:27136
	s_waitcnt lgkmcnt(13)
	v_mfma_f32_32x32x16_bf16 v[82:97], v[186:189], v[150:153], v[82:97]
	v_add_f32_e32 v122, v100, v122
	v_add_f32_e32 v122, v101, v122
	v_add_f32_e32 v122, v102, v122
	v_add_f32_e32 v122, v103, v122
	v_cvt_pk_bf16_f32 v134, v98, v99
	v_cvt_pk_bf16_f32 v135, v100, v101
	ds_read_b64_tr_b16 v[98:99], v217 offset:30720
	ds_read_b64_tr_b16 v[100:101], v217 offset:31232
	s_waitcnt lgkmcnt(14)
	v_mfma_f32_32x32x16_bf16 v[66:81], v[178:181], v[150:153], v[66:81]
	v_add_f32_e32 v122, v104, v122
	v_add_f32_e32 v122, v105, v122
	v_add_f32_e32 v122, v106, v122
	v_add_f32_e32 v122, v107, v122
	v_cvt_pk_bf16_f32 v136, v102, v103
	v_cvt_pk_bf16_f32 v137, v104, v105
	ds_read_b64_tr_b16 v[102:103], v217 offset:27648
	ds_read_b64_tr_b16 v[104:105], v217 offset:28160
	s_waitcnt lgkmcnt(14)
	v_mfma_f32_32x32x16_bf16 v[82:97], v[182:185], v[146:149], v[82:97]
	v_add_f32_e32 v122, v108, v122
	v_add_f32_e32 v122, v109, v122
	v_add_f32_e32 v122, v110, v122
	v_add_f32_e32 v122, v111, v122
	v_cvt_pk_bf16_f32 v130, v106, v107
	v_cvt_pk_bf16_f32 v131, v108, v109
	ds_read_b64_tr_b16 v[106:107], v217 offset:31744
	ds_read_b64_tr_b16 v[108:109], v217 offset:32256
	v_mfma_f32_32x32x16_bf16 v[66:81], v[174:177], v[146:149], v[66:81]
	v_add_f32_e32 v122, v112, v122
	v_add_f32_e32 v122, v113, v122
	v_cvt_pk_bf16_f32 v132, v110, v111
	v_cvt_pk_bf16_f32 v133, v112, v113
	s_nop 0
	v_lshl_add_u64 v[110:111], v[204:205], 0, s[20:21]
	s_add_i32 s26, s38, s35
	s_mov_b32 m0, s26
	s_nop 0
	global_load_lds_dwordx4 v[110:111], off
	v_lshl_add_u64 v[110:111], v[208:209], 0, s[16:17]
	s_add_i32 s26, s40, s34
	s_mov_b32 m0, s26
	s_nop 0
	global_load_lds_dwordx4 v[110:111], off
	v_max_f32_e32 v110, v83, v83
	v_max_f32_e32 v111, v82, v82
	v_max_f32_e32 v110, v111, v110
	s_nop 0
	v_max3_f32 v111, v84, v85, v67
	v_max3_f32 v110, v110, v66, v68
	v_max3_f32 v110, v110, v69, v86
	v_max3_f32 v111, v111, v88, v89
	v_max3_f32 v110, v110, v87, v70
	v_max3_f32 v111, v111, v72, v73
	v_max3_f32 v110, v110, v71, v90
	v_max3_f32 v111, v111, v92, v93
	v_max3_f32 v110, v110, v91, v74
	v_max3_f32 v111, v111, v76, v77
	v_max3_f32 v110, v110, v75, v94
	v_max3_f32 v111, v111, v96, v97
	v_max3_f32 v110, v110, v95, v78
	v_max3_f32 v111, v111, v80, v81
	v_max3_f32 v110, v110, v79, v111
	v_mov_b32_e32 v111, v110
	s_nop 1
	v_permlane32_swap_b32_e32 v110, v111
	v_max_f32_e32 v111, v111, v111
	v_max_f32_e32 v110, v110, v110
	v_max_f32_e32 v110, v110, v111
	v_cmp_lt_f32_e32 vcc, s15, v110
	s_cmp_lg_u64 vcc, 0
	v_add_f32_e32 v201, v201, v122
	s_cselect_b64 s[26:27], -1, 0
	s_cbranch_vccnz .LBB3_14

.LBB3_393:
	s_endpgm
	s_nop 0
	s_nop 0
	s_nop 0
	s_nop 0
	s_nop 0
	s_nop 0
	s_nop 0
	s_nop 0
	s_nop 0
	s_nop 0
	s_nop 0
	s_nop 0
	s_nop 0
	s_nop 0
	s_nop 0
	s_nop 0
	s_nop 0
	s_nop 0
	s_nop 0
	s_nop 0
	s_nop 0
	s_nop 0
	s_nop 0
	s_nop 0
	s_nop 0
	s_nop 0
	s_nop 0
	s_nop 0
	s_nop 0
	s_nop 0
	s_nop 0
	s_nop 0
	s_nop 0
	s_nop 0
	s_nop 0
	s_nop 0
	s_nop 0
	s_nop 0
	s_nop 0
	s_nop 0
	s_nop 0
	s_nop 0
	s_nop 0
	s_nop 0
	s_nop 0
	s_nop 0
	s_nop 0
	s_nop 0
